# background conversion in NSA tile loop v1 (first version, single-buffer, one piece per iteration)
# baseline (speedup 1.0000x reference)
.LBB0_2337:
	s_mov_b32 s99, 0
	s_mov_b32 s32, 0
	v_writelane_b32 v244, s32, 2
	v_mov_b32_e32 v91, v0
	s_nop 0
	v_readfirstlane_b32 s95, v91
	s_ashr_i32 s75, s95, 6
	s_cmp_lt_i32 s75, 4
	s_cbranch_scc1 .LBB0_2339
	s_setprio 1

.LBB0_2419:
	s_lshl_b32 s2, s2, 13
	s_add_i32 s76, s2, 0
	s_add_i32 s76, s76, 0x10000
	s_andn2_b64 vcc, exec, s[8:9]
	v_lshlrev_b32_e32 v134, 2, v162
	s_cbranch_vccnz .LBB0_2468
	v_or_b32_e32 v6, 32, v168
	v_cmp_gt_i32_e64 s[40:41], v6, v2
	v_cmp_lt_i32_e64 s[42:43], v6, v2
	v_or_b32_e32 v6, 34, v168
	v_cmp_gt_i32_e64 s[44:45], v6, v2
	v_or_b32_e32 v6, 35, v168
	v_cmp_gt_i32_e64 s[46:47], v6, v2
	v_or_b32_e32 v6, 40, v168
	v_cmp_gt_i32_e64 s[48:49], v6, v2
	v_or_b32_e32 v6, 41, v168
	v_cmp_gt_i32_e64 s[50:51], v6, v2
	v_or_b32_e32 v6, 42, v168
	v_cmp_gt_i32_e64 s[52:53], v6, v2
	v_or_b32_e32 v6, 43, v168
	v_cmp_gt_i32_e64 s[54:55], v6, v2
	v_or_b32_e32 v6, 48, v168
	v_cmp_gt_i32_e64 s[56:57], v6, v2
	v_or_b32_e32 v6, 49, v168
	v_cmp_gt_i32_e64 s[58:59], v6, v2
	v_or_b32_e32 v6, 50, v168
	v_cmp_gt_i32_e64 s[60:61], v6, v2
	v_or_b32_e32 v6, 51, v168
	v_cmp_gt_i32_e64 s[62:63], v6, v2
	v_or_b32_e32 v6, 56, v168
	v_cmp_gt_i32_e64 s[64:65], v6, v2
	v_or_b32_e32 v6, 57, v168
	v_cmp_gt_i32_e64 s[66:67], v6, v2
	v_or_b32_e32 v6, 58, v168
	v_cmp_gt_i32_e64 s[68:69], v6, v2
	v_or_b32_e32 v6, 59, v168
	v_cmp_gt_i32_e64 s[6:7], v168, v2
	v_cmp_lt_i32_e64 s[8:9], v168, v2
	v_cmp_gt_i32_e64 s[10:11], v135, v2
	v_cmp_gt_i32_e64 s[12:13], v169, v2
	v_cmp_gt_i32_e64 s[14:15], v170, v2
	v_cmp_gt_i32_e64 s[16:17], v171, v2
	v_cmp_gt_i32_e64 s[18:19], v172, v2
	v_cmp_gt_i32_e64 s[20:21], v173, v2
	v_cmp_gt_i32_e64 s[22:23], v174, v2
	v_cmp_gt_i32_e64 s[24:25], v175, v2
	v_cmp_gt_i32_e64 s[26:27], v176, v2
	v_cmp_gt_i32_e64 s[28:29], v177, v2
	v_cmp_gt_i32_e64 s[30:31], v178, v2
	v_cmp_gt_i32_e64 s[34:35], v179, v2
	v_cmp_gt_i32_e64 s[36:37], v180, v2
	v_cmp_gt_i32_e64 s[38:39], v181, v2
	v_cmp_gt_i32_e64 s[70:71], v6, v2
	s_min_u32 s2, s92, 8
	v_lshlrev_b32_e32 v2, 4, v4
	s_add_i32 s2, s92, s2
	v_and_b32_e32 v2, 0xc0, v2
	s_lshl_b32 s87, s2, 13
	v_lshl_or_b32 v2, v160, 8, v2
	v_readlane_b32 s2, v247, 4
	v_lshlrev_b32_e32 v5, 1, v4
	v_mov_b32_e32 v140, 0
	v_add_u32_e32 v185, s2, v2
	v_readlane_b32 s2, v247, 5
	s_movk_i32 s96, 0xc00
	s_add_i32 s91, s91, s92
	v_add_u32_e32 v187, s2, v2
	v_readlane_b32 s2, v247, 6
	s_add_i32 s93, s93, s3
	v_mov_b32_e32 v139, v131
	v_add_u32_e32 v188, s2, v2
	v_readlane_b32 s2, v247, 7
	s_mov_b32 s94, 2
	v_add_u32_e32 v183, s75, v134
	v_add_u32_e32 v189, s2, v2
	v_readlane_b32 s2, v247, 8
	v_add3_u32 v184, s76, v166, v134
	s_lshl_b32 s95, s92, 13
	v_add_u32_e32 v190, s2, v2
	v_readlane_b32 s2, v247, 9
	s_addk_i32 s87, 0x4000
	v_and_or_b32 v186, v5, 32, v3
	v_add_u32_e32 v191, s2, v2
	v_readlane_b32 s2, v247, 10
	s_add_i32 s86, s75, 0xc000
	s_mov_b32 s3, 0
	v_add_u32_e32 v192, s2, v2
	v_readlane_b32 s2, v247, 11
	v_mov_b32_e32 v202, 0
	v_mov_b32_e32 v3, v140
	v_add_u32_e32 v193, s2, v2
	v_readlane_b32 s2, v247, 12
	v_mov_b32_e32 v4, v140
	v_mov_b32_e32 v5, v140
	v_add_u32_e32 v194, s2, v2
	v_readlane_b32 s2, v247, 13
	v_mov_b32_e32 v6, v140
	v_mov_b32_e32 v7, v140
	v_add_u32_e32 v195, s2, v2
	v_readlane_b32 s2, v247, 14
	v_mov_b32_e32 v8, v140
	v_mov_b32_e32 v9, v140
	v_add_u32_e32 v196, s2, v2
	v_readlane_b32 s2, v247, 15
	v_mov_b32_e32 v10, v140
	v_mov_b32_e32 v11, v140
	v_add_u32_e32 v197, s2, v2
	v_readlane_b32 s2, v247, 16
	v_mov_b32_e32 v12, v140
	v_mov_b32_e32 v13, v140
	v_add_u32_e32 v198, s2, v2
	v_readlane_b32 s2, v247, 17
	v_mov_b32_e32 v14, v140
	v_mov_b32_e32 v15, v140
	v_add_u32_e32 v199, s2, v2
	v_readlane_b32 s2, v247, 21
	v_mov_b32_e32 v16, v140
	v_mov_b32_e32 v17, v140
	v_add_u32_e32 v200, s2, v2
	s_add_i32 s2, 0, 0x8000
	v_add_u32_e32 v201, s2, v2
	s_mov_b32 s2, 0
	v_mov_b32_e32 v2, 0
	v_mov_b32_e32 v18, 0
	v_mov_b32_e32 v19, v140
	v_mov_b32_e32 v20, v140
	v_mov_b32_e32 v21, v140
	v_mov_b32_e32 v22, v140
	v_mov_b32_e32 v23, v140
	v_add_u32_e32 v226, v201, v186
	v_mov_b32_e32 v24, v140
	v_mov_b32_e32 v25, v140
	v_mov_b32_e32 v26, v140
	v_mov_b32_e32 v27, v140
	v_mov_b32_e32 v28, v140
	v_mov_b32_e32 v29, v140
	v_mov_b32_e32 v30, v140
	v_mov_b32_e32 v31, v140
	v_mov_b32_e32 v32, v140
	v_mov_b32_e32 v33, v140
	s_mov_b32 s99, 0
	s_mov_b32 s32, 0
	v_writelane_b32 v244, s32, 2
	v_readlane_b32 s72, v249, 50
	s_cmp_gt_i32 s72, 7
	s_cbranch_scc1 .Lbgn_ini
	s_mul_i32 s72, s72, 48
	v_readlane_b32 s73, v248, 47
	s_add_i32 s72, s73, s72
	v_readlane_b32 s73, v248, 48
	s_add_i32 s78, s72, 48
	s_min_i32 s73, s73, s78
	s_min_i32 s73, s73, 0x1be90
	v_readlane_b32 s78, v249, 16
	s_add_i32 s72, s72, s78
	s_cmp_ge_i32 s72, s73
	s_cbranch_scc1 .Lbgn_ini
	v_writelane_b32 v244, s73, 3
	s_sub_i32 s98, s72, 8
	s_mov_b32 s99, 0x36
.Lbgn_ini:
	s_branch .LBB0_2422
.LBB0_2421:
	s_or_b64 exec, exec, s[72:73]
	s_waitcnt lgkmcnt(0)
	v_add_u32_e32 v34, s75, v136
	ds_read_b32 v35, v34 offset:57472
	v_pk_add_f32 v[112:113], v[140:141], v[64:65] op_sel_hi:[0,1]
	v_pk_add_f32 v[110:111], v[140:141], v[62:63] op_sel_hi:[0,1]
	v_pk_add_f32 v[108:109], v[140:141], v[60:61] op_sel_hi:[0,1]
	v_pk_add_f32 v[106:107], v[140:141], v[58:59] op_sel_hi:[0,1]
	s_waitcnt lgkmcnt(0)
	v_mul_f32_e32 v2, v2, v35
	v_mul_f32_e32 v18, v18, v35
	ds_write2_b32 v184, v2, v18 offset1:32
	ds_read_b32 v2, v34 offset:57476
	v_pk_add_f32 v[104:105], v[140:141], v[56:57] op_sel_hi:[0,1]
	v_pk_add_f32 v[102:103], v[140:141], v[54:55] op_sel_hi:[0,1]
	v_pk_add_f32 v[100:101], v[140:141], v[52:53] op_sel_hi:[0,1]
	v_pk_add_f32 v[98:99], v[140:141], v[50:51] op_sel_hi:[0,1]
	s_waitcnt lgkmcnt(0)
	v_mul_f32_e32 v3, v3, v2
	v_mul_f32_e32 v2, v19, v2
	ds_write2_b32 v184, v3, v2 offset0:64 offset1:96
	ds_read_b32 v2, v34 offset:57480
	s_waitcnt lgkmcnt(0)
	v_mul_f32_e32 v3, v4, v2
	v_mul_f32_e32 v2, v20, v2
	ds_write2_b32 v184, v3, v2 offset0:128 offset1:160
	ds_read_b32 v2, v34 offset:57484
	v_add_u32_e32 v4, 0x800, v184
	s_waitcnt lgkmcnt(0)
	v_mul_f32_e32 v3, v5, v2
	v_mul_f32_e32 v2, v21, v2
	ds_write2_b32 v184, v3, v2 offset0:192 offset1:224
	ds_read_b32 v2, v34 offset:57504
	s_waitcnt lgkmcnt(0)
	v_mul_f32_e32 v3, v6, v2
	v_mul_f32_e32 v2, v22, v2
	ds_write2_b32 v4, v3, v2 offset1:32
	ds_read_b32 v2, v34 offset:57508
	s_waitcnt lgkmcnt(0)
	v_mul_f32_e32 v3, v7, v2
	v_mul_f32_e32 v2, v23, v2
	ds_write2_b32 v4, v3, v2 offset0:64 offset1:96
	ds_read_b32 v2, v34 offset:57512
	s_waitcnt lgkmcnt(0)
	v_mul_f32_e32 v3, v8, v2
	v_mul_f32_e32 v2, v24, v2
	ds_write2_b32 v4, v3, v2 offset0:128 offset1:160
	ds_read_b32 v2, v34 offset:57516
	s_waitcnt lgkmcnt(0)
	v_mul_f32_e32 v3, v9, v2
	v_mul_f32_e32 v2, v25, v2
	ds_write2_b32 v4, v3, v2 offset0:192 offset1:224
	ds_read_b32 v2, v34 offset:57536
	v_add_u32_e32 v4, 0x1000, v184
	s_waitcnt lgkmcnt(0)
	v_mul_f32_e32 v3, v10, v2
	v_mul_f32_e32 v2, v26, v2
	ds_write2_b32 v4, v3, v2 offset1:32
	ds_read_b32 v2, v34 offset:57540
	s_waitcnt lgkmcnt(0)
	v_mul_f32_e32 v3, v11, v2
	v_mul_f32_e32 v2, v27, v2
	ds_write2_b32 v4, v3, v2 offset0:64 offset1:96
	ds_read_b32 v2, v34 offset:57544
	s_waitcnt lgkmcnt(0)
	v_mul_f32_e32 v3, v12, v2
	v_mul_f32_e32 v2, v28, v2
	ds_write2_b32 v4, v3, v2 offset0:128 offset1:160
	ds_read_b32 v2, v34 offset:57548
	s_waitcnt lgkmcnt(0)
	v_mul_f32_e32 v3, v13, v2
	v_mul_f32_e32 v2, v29, v2
	ds_write2_b32 v4, v3, v2 offset0:192 offset1:224
	ds_read_b32 v2, v34 offset:57568
	v_add_u32_e32 v4, 0x1800, v184
	s_waitcnt lgkmcnt(0)
	v_mul_f32_e32 v3, v14, v2
	v_mul_f32_e32 v2, v30, v2
	ds_write2_b32 v4, v3, v2 offset1:32
	ds_read_b32 v2, v34 offset:57572
	s_waitcnt lgkmcnt(0)
	v_mul_f32_e32 v3, v15, v2
	v_mul_f32_e32 v2, v31, v2
	ds_write2_b32 v4, v3, v2 offset0:64 offset1:96
	ds_read_b32 v2, v34 offset:57576
	s_waitcnt lgkmcnt(0)
	v_mul_f32_e32 v3, v16, v2
	v_mul_f32_e32 v2, v32, v2
	ds_write2_b32 v4, v3, v2 offset0:128 offset1:160
	ds_read_b32 v2, v34 offset:57580
	v_mov_b64_e32 v[34:35], v[66:67]
	v_mov_b64_e32 v[36:37], v[68:69]
	v_mov_b64_e32 v[38:39], v[70:71]
	v_mov_b64_e32 v[40:41], v[72:73]
	s_waitcnt lgkmcnt(0)
	v_mul_f32_e32 v3, v17, v2
	v_mul_f32_e32 v2, v33, v2
	ds_write2_b32 v4, v3, v2 offset0:192 offset1:224
	s_waitcnt lgkmcnt(0)
	v_mov_b32_e32 v17, 0
	v_mov_b64_e32 v[42:43], v[74:75]
	v_mov_b64_e32 v[44:45], v[76:77]
	v_mov_b64_e32 v[46:47], v[78:79]
	v_mov_b64_e32 v[48:49], v[80:81]
	v_mov_b32_e32 v16, v17
	v_mov_b32_e32 v15, v17
	v_mov_b32_e32 v14, v17
	v_mov_b32_e32 v13, v17
	v_mov_b32_e32 v12, v17
	v_mov_b32_e32 v11, v17
	v_mov_b32_e32 v10, v17
	v_mov_b32_e32 v9, v17
	v_mov_b32_e32 v8, v17
	v_mov_b32_e32 v7, v17
	v_mov_b32_e32 v6, v17
	v_mov_b32_e32 v5, v17
	v_mov_b32_e32 v4, v17
	v_mov_b32_e32 v3, v17
	v_mov_b32_e32 v2, v17
	v_mov_b32_e32 v33, v17
	v_mov_b32_e32 v32, v17
	v_mov_b32_e32 v31, v17
	v_mov_b32_e32 v30, v17
	v_mov_b32_e32 v29, v17
	v_mov_b32_e32 v28, v17
	v_mov_b32_e32 v27, v17
	v_mov_b32_e32 v26, v17
	v_mov_b32_e32 v25, v17
	v_mov_b32_e32 v24, v17
	v_mov_b32_e32 v23, v17
	v_mov_b32_e32 v22, v17
	v_mov_b32_e32 v21, v17
	v_mov_b32_e32 v20, v17
	v_mov_b32_e32 v19, v17
	v_mov_b32_e32 v18, v17
	v_mov_b32_e32 v140, v17
	v_mov_b32_e32 v202, v17
	s_addk_i32 s2, 0x2000
	s_add_i32 s94, s94, 1
	s_cmp_eq_u32 s87, s2
	s_cbranch_scc1 .LBB0_2467
.LBB0_2422:
	s_bitcmp1_b32 s99, 4
	s_cbranch_scc0 .Lbgn_end
	s_mov_b32 s85, m0
	v_readlane_b32 s84, v249, 16
	v_and_b32_e32 v50, 63, v0
	v_and_b32_e32 v51, 31, v50
	v_lshrrev_b32_e32 v52, 5, v50
	s_lshl_b32 s84, s84, 11
	s_add_i32 s84, s84, 0x24000
	s_bitcmp1_b32 s99, 5
	s_cbranch_scc1 .Lbgn_adv
	s_cmp_eq_u32 s32, 3
	s_cbranch_scc1 .Lbgn_w2
	s_cmp_eq_u32 s32, 0
	s_cbranch_scc1 .Lbgn_w0
	s_waitcnt vmcnt(1)
	s_branch .Lbgn_wd
.Lbgn_w0:
	s_waitcnt vmcnt(0)
	s_branch .Lbgn_wd

.Lbgn_wd:
	v_lshlrev_b32_e32 v53, 10, v52
	v_lshl_add_u32 v53, v51, 2, v53
	v_add_u32_e32 v53, s84, v53
	ds_read2_b32 v[54:55], v53 offset1:32
	ds_read2_b32 v[56:57], v53 offset0:64 offset1:96
	ds_read2_b32 v[58:59], v53 offset0:128 offset1:160
	ds_read2_b32 v[60:61], v53 offset0:192 offset1:224
	v_mov_b32_e32 v62, 0x42800000
	v_mov_b32_e32 v63, 0x42800000
	s_bitcmp1_b32 s99, 0
	s_cselect_b32 s97, 9, 11
	v_lshlrev_b32_e32 v53, s97, v51
	v_lshl_add_u32 v53, v52, 3, v53
	s_waitcnt lgkmcnt(0)
	v_pk_mul_f32 v[54:55], v[54:55], v[62:63]
	v_pk_mul_f32 v[56:57], v[56:57], v[62:63]
	v_pk_mul_f32 v[58:59], v[58:59], v[62:63]
	v_pk_mul_f32 v[60:61], v[60:61], v[62:63]
	v_cvt_pk_fp8_f32 v64, v54, v55
	v_cvt_pk_fp8_f32 v65, v58, v59
	v_cvt_pk_fp8_f32 v64, v56, v57 op_sel:[0,0,1]
	v_cvt_pk_fp8_f32 v65, v60, v61 op_sel:[0,0,1]
	s_nop 0
	global_store_dwordx2 v53, v[64:65], s[100:101]
	v_readlane_b32 s72, v244, 2
	s_add_i32 s72, s72, 1
	s_nop 0
	v_writelane_b32 v244, s72, 2
.Lbgn_adv:
	s_and_b32 s72, s99, 6
	s_cmp_eq_u32 s72, 6
	s_cbranch_scc1 .Lbgn_new
	s_add_i32 s99, s99, 2
	s_mov_b32 s97, 0x8000
	s_bitcmp1_b32 s99, 0
	s_cselect_b32 s97, 0x20000, s97
	v_readlane_b32 s80, v244, 0
	v_readlane_b32 s81, v244, 1
	s_add_u32 s80, s80, s97
	s_addc_u32 s81, s81, 0
	s_add_u32 s100, s100, 16
	s_addc_u32 s101, s101, 0
	s_branch .Lbgn_save
.Lbgn_new:
	s_add_i32 s72, s98, 8
	v_readlane_b32 s73, v244, 3
	s_cmp_ge_i32 s72, s73
	s_cbranch_scc0 .Lbgn_dec
	s_andn2_b32 s99, s99, 0x10
	s_branch .Lbgn_end
.Lbgn_dec:
	s_mov_b32 s98, s72
	s_andn2_b32 s99, s99, 6
	v_readlane_b32 s82, v249, 1
	v_readlane_b32 s83, v249, 2
	s_sub_u32 s72, s98, 0x3e90
	s_lshr_b32 vcc_lo, s72, 15
	s_and_b32 s72, s72, 0x7fff
	s_lshl_b32 vcc_hi, vcc_lo, 3
	s_addk_i32 vcc_hi, 0xa8
	s_load_dwordx2 s[80:81], s[82:83], vcc_hi
	s_load_dwordx2 s[78:79], s[82:83], 0xe0
	s_lshr_b32 vcc_hi, s72, 9
	s_and_b32 s72, s72, 0x1ff
	s_cmp_eq_u32 vcc_lo, 2
	s_cbranch_scc1 .Lbgn_dn
	s_lshr_b32 s73, s72, 4
	s_and_b32 s72, s72, 15
	s_lshl_b32 s100, vcc_hi, 21
	s_lshl_b32 s101, vcc_hi, 22
	s_lshl_b32 vcc_hi, s73, 6
	s_add_u32 s100, s100, vcc_hi
	s_lshl_b32 vcc_hi, s73, 17
	s_add_u32 s101, s101, vcc_hi
	s_lshl_b32 vcc_hi, s72, 7
	s_add_u32 s101, s101, vcc_hi
	s_lshr_b32 vcc_hi, s72, 2
	s_lshl_b32 vcc_hi, vcc_hi, 19
	s_add_u32 s100, s100, vcc_hi
	s_and_b32 vcc_hi, s72, 3
	s_lshl_b32 vcc_hi, vcc_hi, 16
	s_add_u32 s100, s100, vcc_hi
	s_lshl_b32 vcc_hi, vcc_lo, 18
	s_add_u32 s100, s100, vcc_hi
	s_add_u32 s100, s100, 0x1b000000
	s_bitset0_b32 s99, 0
	s_branch .Lbgn_dd
.Lbgn_dn:
	s_lshr_b32 s73, s72, 6
	s_and_b32 s72, s72, 63
	s_lshl_b32 s100, vcc_hi, 20
	s_lshl_b32 s101, vcc_hi, 22
	s_lshl_b32 vcc_hi, s73, 6
	s_add_u32 s100, s100, vcc_hi
	s_lshl_b32 vcc_hi, s73, 19
	s_add_u32 s101, s101, vcc_hi
	s_lshl_b32 vcc_hi, s72, 7
	s_add_u32 s101, s101, vcc_hi
	s_lshl_b32 vcc_hi, s72, 14
	s_add_u32 s100, s100, vcc_hi
	s_add_u32 s100, s100, 0x2000000
	s_bitset1_b32 s99, 0
.Lbgn_dd:
	s_waitcnt lgkmcnt(0)
	s_add_u32 s80, s80, s101
	s_addc_u32 s81, s81, 0
	s_add_u32 s100, s78, s100
	s_addc_u32 s101, s79, 0
.Lbgn_save:
	v_writelane_b32 v244, s80, 0
	v_writelane_b32 v244, s81, 1
.Lbgn_issue:
	v_lshrrev_b32_e32 v54, 3, v50
	v_and_b32_e32 v55, 7, v50
	v_lshlrev_b32_e32 v55, 4, v55
	s_mov_b32 s72, 0x4000
	s_bitcmp1_b32 s99, 0
	s_cselect_b32 s97, 13, 11
	s_cselect_b32 s72, 0x10000, s72
	v_lshlrev_b32_e32 v54, s97, v54
	v_add_u32_e32 v54, v54, v55
	s_mov_b32 m0, s84
	s_bitcmp1_b32 s99, 5
	s_cbranch_scc0 .Lbgn_i2
	global_load_lds_dwordx4 v54, s[80:81] nt
.Lbgn_i2:
	global_load_lds_dwordx4 v54, s[80:81] nt
	s_add_i32 m0, m0, 0x400
	s_add_u32 s80, s80, s72
	s_addc_u32 s81, s81, 0
	global_load_lds_dwordx4 v54, s[80:81] nt
	s_andn2_b32 s99, s99, 0x20
	s_mov_b32 s32, 0
	s_mov_b32 m0, s85
.Lbgn_end:
	s_mul_hi_u32 s97, s3, 0xaaaaaaab
	s_lshr_b32 s97, s97, 1
	s_mulk_i32 s97, 0xa000
	s_add_i32 s97, s97, s2
	v_add_u32_e32 v225, s97, v226
	s_add_i32 s80, s3, 2
	s_cmp_lt_u32 s80, s90
	s_cselect_b64 s[72:73], -1, 0
	s_cmp_ge_u32 s80, s90
	s_mov_b64 s[78:79], -1
	s_cbranch_scc0 .LBB0_2430
	s_cmp_ge_u32 s3, s91
	s_cbranch_scc0 .LBB0_2425
	s_bitcmp1_b32 s99, 4
	s_cbranch_scc1 .Lbgn_h0a
	s_waitcnt vmcnt(0) lgkmcnt(0)
	s_branch .Lbgn_h0b
.Lbgn_h0a:
	s_waitcnt vmcnt(3) lgkmcnt(0)
.Lbgn_h0b:
	s_barrier
	s_mov_b64 s[78:79], 0
.LBB0_2425:
	s_andn2_b64 vcc, exec, s[78:79]
	s_cbranch_vccnz .LBB0_2427
	s_bitcmp1_b32 s99, 4
	s_cbranch_scc1 .Lbgn_h1a
	s_waitcnt vmcnt(1) lgkmcnt(0)
	s_branch .Lbgn_h1b
.Lbgn_h1a:
	s_waitcnt vmcnt(4) lgkmcnt(0)
.Lbgn_h1b:
	s_barrier

.LBB0_2429:
	s_cmp_gt_u32 s78, s92
	s_cselect_b64 s[78:79], -1, 0
	s_and_b64 s[78:79], s[78:79], exec
	s_cselect_b32 s79, s93, 0
	s_cselect_b32 s78, s96, 0xa00
	s_add_i32 s79, s79, s3
	s_lshl_b32 s79, s79, 6
	s_addk_i32 s79, 0xc0
	s_mul_hi_i32 s81, s79, 0x4e00
	s_mulk_i32 s79, 0x4e00
	s_add_u32 s79, s0, s79
	s_addc_u32 s81, s1, s81
	s_add_u32 s78, s79, s78
	s_addc_u32 s79, s81, 0
	v_lshl_add_u64 v[50:51], s[78:79], 0, v[130:131]
	s_add_i32 s78, s2, 0x6000
	s_and_b32 s78, s78, 0x6000
	s_add_i32 s78, s78, s75
	s_mov_b32 s79, m0
	s_mov_b32 m0, s78
	s_nop 0
	global_load_lds_dwordx4 v[50:51], off
	s_mov_b32 m0, s79
	s_bitset1_b32 s32, 0
	s_andn2_b64 vcc, exec, s[72:73]
	s_cbranch_vccz .LBB0_2433
	s_branch .LBB0_2434

.LBB0_2431:
	s_bitcmp1_b32 s99, 4
	s_cbranch_scc1 .Lbgn_h2a
	s_waitcnt vmcnt(2) lgkmcnt(0)
	s_branch .Lbgn_h2b

.Lbgn_h2b:
	s_barrier
	s_add_i32 s78, s3, 3
	s_cmp_ge_u32 s78, s90
	s_cbranch_scc0 .LBB0_2429

.LBB0_2433:
	s_mul_hi_u32 s72, s94, 0xaaaaaaab
	s_lshr_b32 s72, s72, 1
	s_mulk_i32 s72, 0x6000
	s_sub_i32 s78, s86, s72
	s_cmp_gt_u32 s80, s92
	s_cselect_b64 s[72:73], -1, 0
	s_and_b64 s[72:73], s[72:73], exec
	s_movk_i32 s72, 0x1c00
	s_cselect_b32 s73, s93, 0
	s_cselect_b32 s72, s72, 0x1a00
	s_add_i32 s73, s73, s3
	s_lshl_b32 s73, s73, 6
	s_addk_i32 s73, 0x80
	s_mul_hi_i32 s79, s73, 0x4e00
	s_mulk_i32 s73, 0x4e00
	s_add_u32 s73, s0, s73
	s_addc_u32 s79, s1, s79
	s_add_u32 s72, s73, s72
	s_addc_u32 s73, s79, 0
	v_lshl_add_u64 v[50:51], s[72:73], 0, v[138:139]
	s_add_i32 s72, s2, s78
	s_mov_b32 s73, m0
	s_mov_b32 m0, s72
	s_nop 0
	global_load_lds_dwordx4 v[50:51], off
	s_mov_b32 m0, s73
	s_bitset1_b32 s32, 1

.LBB0_2471:
	s_or_b64 exec, exec, s[6:7]
	s_waitcnt lgkmcnt(0)
	v_lshl_add_u32 v51, v160, 4, s75
	v_add3_u32 v50, s76, v166, v134
	ds_read_b32 v54, v51 offset:57472
	ds_read2_b32 v[52:53], v50 offset1:32
	s_lshl_b32 s2, s2, 1
	v_readlane_b32 s3, v249, 61
	s_add_u32 s2, s3, s2
	v_readlane_b32 s3, v249, 36
	s_waitcnt lgkmcnt(0)
	v_fma_f32 v2, v2, v54, v52
	v_fmac_f32_e32 v53, v18, v54
	ds_write2_b32 v50, v2, v53 offset1:32
	ds_read_b32 v2, v51 offset:57476
	ds_read2_b32 v[52:53], v50 offset0:64 offset1:96
	s_addc_u32 s3, s3, 0
	s_waitcnt lgkmcnt(0)
	v_fma_f32 v3, v3, v2, v52
	v_fmac_f32_e32 v53, v19, v2
	ds_write2_b32 v50, v3, v53 offset0:64 offset1:96
	ds_read_b32 v18, v51 offset:57480
	ds_read2_b32 v[2:3], v50 offset0:128 offset1:160
	v_add_u32_e32 v19, 0x1000, v50
	s_waitcnt lgkmcnt(0)
	v_fma_f32 v2, v4, v18, v2
	v_fmac_f32_e32 v3, v20, v18
	ds_write2_b32 v50, v2, v3 offset0:128 offset1:160
	ds_read_b32 v4, v51 offset:57484
	ds_read2_b32 v[2:3], v50 offset0:192 offset1:224
	v_add_u32_e32 v18, 0x800, v50
	v_add_u32_e32 v20, 0x1800, v50
	s_waitcnt lgkmcnt(0)
	v_fma_f32 v2, v5, v4, v2
	v_fmac_f32_e32 v3, v21, v4
	ds_write2_b32 v50, v2, v3 offset0:192 offset1:224
	ds_read_b32 v4, v51 offset:57504
	ds_read2_b32 v[2:3], v18 offset1:32
	s_waitcnt lgkmcnt(0)
	v_fma_f32 v2, v6, v4, v2
	v_fmac_f32_e32 v3, v22, v4
	ds_write2_b32 v18, v2, v3 offset1:32
	ds_read_b32 v4, v51 offset:57508
	ds_read2_b32 v[2:3], v18 offset0:64 offset1:96
	s_waitcnt lgkmcnt(0)
	v_fma_f32 v2, v7, v4, v2
	v_fmac_f32_e32 v3, v23, v4
	ds_write2_b32 v18, v2, v3 offset0:64 offset1:96
	ds_read_b32 v4, v51 offset:57512
	ds_read2_b32 v[2:3], v18 offset0:128 offset1:160
	s_waitcnt lgkmcnt(0)
	v_fma_f32 v2, v8, v4, v2
	v_fmac_f32_e32 v3, v24, v4
	ds_write2_b32 v18, v2, v3 offset0:128 offset1:160
	ds_read_b32 v4, v51 offset:57516
	ds_read2_b32 v[2:3], v18 offset0:192 offset1:224
	s_waitcnt lgkmcnt(0)
	v_fma_f32 v2, v9, v4, v2
	v_fmac_f32_e32 v3, v25, v4
	ds_write2_b32 v18, v2, v3 offset0:192 offset1:224
	ds_read_b32 v4, v51 offset:57536
	ds_read2_b32 v[2:3], v19 offset1:32
	s_waitcnt lgkmcnt(0)
	v_fma_f32 v2, v10, v4, v2
	v_fmac_f32_e32 v3, v26, v4
	ds_write2_b32 v19, v2, v3 offset1:32
	ds_read_b32 v4, v51 offset:57540
	ds_read2_b32 v[2:3], v19 offset0:64 offset1:96
	s_waitcnt lgkmcnt(0)
	v_fma_f32 v2, v11, v4, v2
	v_fmac_f32_e32 v3, v27, v4
	ds_write2_b32 v19, v2, v3 offset0:64 offset1:96
	ds_read_b32 v4, v51 offset:57544
	ds_read2_b32 v[2:3], v19 offset0:128 offset1:160
	s_waitcnt lgkmcnt(0)
	v_fma_f32 v2, v12, v4, v2
	v_fmac_f32_e32 v3, v28, v4
	ds_write2_b32 v19, v2, v3 offset0:128 offset1:160
	ds_read_b32 v4, v51 offset:57548
	ds_read2_b32 v[2:3], v19 offset0:192 offset1:224
	s_waitcnt lgkmcnt(0)
	v_fma_f32 v2, v13, v4, v2
	v_fmac_f32_e32 v3, v29, v4
	ds_write2_b32 v19, v2, v3 offset0:192 offset1:224
	ds_read_b32 v4, v51 offset:57568
	ds_read2_b32 v[2:3], v20 offset1:32
	s_waitcnt lgkmcnt(0)
	v_fma_f32 v2, v14, v4, v2
	v_fmac_f32_e32 v3, v30, v4
	ds_write2_b32 v20, v2, v3 offset1:32
	ds_read_b32 v4, v51 offset:57572
	ds_read2_b32 v[2:3], v20 offset0:64 offset1:96
	s_waitcnt lgkmcnt(0)
	v_fma_f32 v2, v15, v4, v2
	v_fmac_f32_e32 v3, v31, v4
	ds_write2_b32 v20, v2, v3 offset0:64 offset1:96
	ds_read_b32 v4, v51 offset:57576
	ds_read2_b32 v[2:3], v20 offset0:128 offset1:160
	s_waitcnt lgkmcnt(0)
	v_fma_f32 v2, v16, v4, v2
	v_fmac_f32_e32 v3, v32, v4
	ds_write2_b32 v20, v2, v3 offset0:128 offset1:160
	ds_read_b32 v4, v51 offset:57580
	ds_read2_b32 v[2:3], v20 offset0:192 offset1:224
	s_waitcnt lgkmcnt(0)
	v_fma_f32 v2, v17, v4, v2
	v_fmac_f32_e32 v3, v33, v4
	ds_write2_b32 v20, v2, v3 offset0:192 offset1:224
	v_mov_b64_e32 v[2:3], v[66:67]
	s_waitcnt lgkmcnt(0)
	v_mov_b64_e32 v[4:5], v[68:69]
	v_mov_b64_e32 v[6:7], v[70:71]
	v_mov_b64_e32 v[8:9], v[72:73]
	v_mov_b64_e32 v[10:11], v[74:75]
	v_mov_b64_e32 v[12:13], v[76:77]
	v_mov_b64_e32 v[14:15], v[78:79]
	v_mov_b64_e32 v[16:17], v[80:81]
	ds_read2_b32 v[2:3], v50 offset1:32
	s_waitcnt vmcnt(31) lgkmcnt(0)
	v_add_f32_e32 v4, v96, v2
	s_waitcnt vmcnt(30)
	v_add_f32_e32 v5, v97, v3
	ds_read2_b32 v[2:3], v50 offset0:64 offset1:96
	s_waitcnt vmcnt(29) lgkmcnt(0)
	v_add_f32_e32 v6, v94, v2
	s_waitcnt vmcnt(28)
	v_add_f32_e32 v7, v95, v3
	ds_read2_b32 v[2:3], v50 offset0:128 offset1:160
	s_waitcnt vmcnt(27) lgkmcnt(0)
	v_add_f32_e32 v8, v92, v2
	s_waitcnt vmcnt(26)
	v_add_f32_e32 v9, v93, v3
	ds_read2_b32 v[2:3], v50 offset0:192 offset1:224
	s_waitcnt vmcnt(25) lgkmcnt(0)
	v_add_f32_e32 v10, v90, v2
	s_waitcnt vmcnt(24)
	v_add_f32_e32 v11, v91, v3
	ds_read2_b32 v[2:3], v18 offset1:32
	s_waitcnt vmcnt(23) lgkmcnt(0)
	v_add_f32_e32 v12, v86, v2
	s_waitcnt vmcnt(22)
	v_add_f32_e32 v13, v87, v3
	ds_read2_b32 v[2:3], v18 offset0:64 offset1:96
	s_waitcnt vmcnt(21) lgkmcnt(0)
	v_add_f32_e32 v14, v84, v2
	s_waitcnt vmcnt(20)
	v_add_f32_e32 v15, v85, v3
	ds_read2_b32 v[2:3], v18 offset0:128 offset1:160
	s_waitcnt vmcnt(19) lgkmcnt(0)
	v_add_f32_e32 v16, v82, v2
	s_waitcnt vmcnt(18)
	v_add_f32_e32 v17, v83, v3
	ds_read2_b32 v[2:3], v18 offset0:192 offset1:224
	s_waitcnt vmcnt(17) lgkmcnt(0)
	v_add_f32_e32 v18, v46, v2
	s_waitcnt vmcnt(16)
	v_add_f32_e32 v21, v47, v3
	ds_read2_b32 v[2:3], v19 offset1:32
	s_waitcnt vmcnt(15) lgkmcnt(0)
	v_add_f32_e32 v22, v58, v2
	s_waitcnt vmcnt(14)
	v_add_f32_e32 v23, v59, v3
	ds_read2_b32 v[2:3], v19 offset0:64 offset1:96
	s_waitcnt vmcnt(13) lgkmcnt(0)
	v_add_f32_e32 v24, v48, v2
	s_waitcnt vmcnt(12)
	v_add_f32_e32 v25, v49, v3
	ds_read2_b32 v[2:3], v19 offset0:128 offset1:160
	s_waitcnt vmcnt(11) lgkmcnt(0)
	v_add_f32_e32 v26, v44, v2
	s_waitcnt vmcnt(10)
	v_add_f32_e32 v27, v45, v3
	ds_read2_b32 v[2:3], v19 offset0:192 offset1:224
	s_waitcnt vmcnt(9) lgkmcnt(0)
	v_add_f32_e32 v19, v40, v2
	s_waitcnt vmcnt(8)
	v_add_f32_e32 v28, v41, v3
	ds_read2_b32 v[2:3], v20 offset1:32
	s_waitcnt vmcnt(7) lgkmcnt(0)
	v_add_f32_e32 v29, v42, v2
	s_waitcnt vmcnt(6)
	v_add_f32_e32 v30, v43, v3
	ds_read2_b32 v[2:3], v20 offset0:64 offset1:96
	s_waitcnt vmcnt(5) lgkmcnt(0)
	v_add_f32_e32 v31, v38, v2
	s_waitcnt vmcnt(4)
	v_add_f32_e32 v32, v39, v3
	ds_read2_b32 v[2:3], v20 offset0:128 offset1:160
	s_waitcnt vmcnt(3) lgkmcnt(0)
	v_add_f32_e32 v33, v36, v2
	s_waitcnt vmcnt(2)
	v_add_f32_e32 v36, v37, v3
	ds_read2_b32 v[2:3], v20 offset0:192 offset1:224
	v_lshlrev_b32_e32 v20, 9, v160
	s_waitcnt lgkmcnt(0)
	s_waitcnt vmcnt(1) lgkmcnt(0)
	v_add_f32_e32 v2, v34, v2
	v_lshlrev_b32_e32 v34, 1, v162
	v_add3_u32 v20, s76, v20, v34
	v_bfe_u32 v34, v4, 16, 1
	v_add3_u32 v4, v4, v34, s74
	ds_write_b16_d16_hi v20, v4
	v_bfe_u32 v4, v5, 16, 1
	v_add3_u32 v4, v5, v4, s74
	ds_write_b16_d16_hi v20, v4 offset:64
	v_bfe_u32 v4, v6, 16, 1
	v_add3_u32 v4, v6, v4, s74
	ds_write_b16_d16_hi v20, v4 offset:128
	v_bfe_u32 v4, v7, 16, 1
	v_add3_u32 v4, v7, v4, s74
	ds_write_b16_d16_hi v20, v4 offset:192
	v_bfe_u32 v4, v8, 16, 1
	v_add3_u32 v4, v8, v4, s74
	ds_write_b16_d16_hi v20, v4 offset:256
	v_bfe_u32 v4, v9, 16, 1
	v_add3_u32 v4, v9, v4, s74
	ds_write_b16_d16_hi v20, v4 offset:320
	v_bfe_u32 v4, v10, 16, 1
	v_add3_u32 v4, v10, v4, s74
	ds_write_b16_d16_hi v20, v4 offset:384
	v_bfe_u32 v4, v11, 16, 1
	v_add3_u32 v4, v11, v4, s74
	ds_write_b16_d16_hi v20, v4 offset:448
	v_bfe_u32 v4, v12, 16, 1
	v_add3_u32 v4, v12, v4, s74
	ds_write_b16_d16_hi v20, v4 offset:1024
	v_bfe_u32 v4, v13, 16, 1
	v_add3_u32 v4, v13, v4, s74
	ds_write_b16_d16_hi v20, v4 offset:1088
	v_bfe_u32 v4, v14, 16, 1
	v_add3_u32 v4, v14, v4, s74
	ds_write_b16_d16_hi v20, v4 offset:1152
	v_bfe_u32 v4, v15, 16, 1
	v_add3_u32 v4, v15, v4, s74
	ds_write_b16_d16_hi v20, v4 offset:1216
	v_bfe_u32 v4, v16, 16, 1
	v_add3_u32 v4, v16, v4, s74
	ds_write_b16_d16_hi v20, v4 offset:1280
	v_bfe_u32 v4, v17, 16, 1
	v_add3_u32 v4, v17, v4, s74
	ds_write_b16_d16_hi v20, v4 offset:1344
	v_bfe_u32 v4, v18, 16, 1
	v_add3_u32 v4, v18, v4, s74
	ds_write_b16_d16_hi v20, v4 offset:1408
	v_bfe_u32 v4, v21, 16, 1
	v_add3_u32 v4, v21, v4, s74
	ds_write_b16_d16_hi v20, v4 offset:1472
	v_bfe_u32 v4, v22, 16, 1
	v_add3_u32 v4, v22, v4, s74
	ds_write_b16_d16_hi v20, v4 offset:2048
	v_bfe_u32 v4, v23, 16, 1
	v_add3_u32 v4, v23, v4, s74
	ds_write_b16_d16_hi v20, v4 offset:2112
	v_bfe_u32 v4, v24, 16, 1
	v_add3_u32 v4, v24, v4, s74
	ds_write_b16_d16_hi v20, v4 offset:2176
	v_bfe_u32 v4, v25, 16, 1
	v_add3_u32 v4, v25, v4, s74
	ds_write_b16_d16_hi v20, v4 offset:2240
	v_bfe_u32 v4, v26, 16, 1
	v_add3_u32 v4, v26, v4, s74
	ds_write_b16_d16_hi v20, v4 offset:2304
	v_bfe_u32 v4, v27, 16, 1
	v_add3_u32 v4, v27, v4, s74
	ds_write_b16_d16_hi v20, v4 offset:2368
	v_bfe_u32 v4, v19, 16, 1
	v_add3_u32 v4, v19, v4, s74
	ds_write_b16_d16_hi v20, v4 offset:2432
	v_bfe_u32 v4, v28, 16, 1
	v_add3_u32 v4, v28, v4, s74
	ds_write_b16_d16_hi v20, v4 offset:2496
	v_bfe_u32 v4, v29, 16, 1
	v_add3_u32 v4, v29, v4, s74
	ds_write_b16_d16_hi v20, v4 offset:3072
	v_bfe_u32 v4, v30, 16, 1
	v_add3_u32 v4, v30, v4, s74
	ds_write_b16_d16_hi v20, v4 offset:3136
	v_bfe_u32 v4, v31, 16, 1
	v_add3_u32 v4, v31, v4, s74
	ds_write_b16_d16_hi v20, v4 offset:3200
	v_bfe_u32 v4, v32, 16, 1
	v_add3_u32 v4, v32, v4, s74
	ds_write_b16_d16_hi v20, v4 offset:3264
	v_bfe_u32 v4, v33, 16, 1
	v_add3_u32 v4, v33, v4, s74
	ds_write_b16_d16_hi v20, v4 offset:3328
	v_bfe_u32 v4, v36, 16, 1
	v_add3_u32 v4, v36, v4, s74
	ds_write_b16_d16_hi v20, v4 offset:3392
	v_bfe_u32 v4, v2, 16, 1
	s_waitcnt vmcnt(0)
	v_add_f32_e32 v3, v35, v3
	v_add3_u32 v2, v2, v4, s74
	ds_write_b16_d16_hi v20, v2 offset:3456
	v_bfe_u32 v2, v3, 16, 1
	v_add3_u32 v2, v3, v2, s74
	ds_write_b16_d16_hi v20, v2 offset:3520
	v_lshlrev_b32_e32 v2, 1, v158
	v_and_b32_e32 v130, 0x70, v2
	s_waitcnt lgkmcnt(0)
	v_lshrrev_b32_e32 v12, 3, v137
	v_add_u32_e32 v13, s76, v130
	v_lshl_add_u32 v2, v12, 7, v13
	ds_read_b128 v[2:5], v2
	v_or_b32_e32 v8, s0, v12
	v_mov_b32_e32 v9, s1
	v_lshl_add_u64 v[6:7], s[2:3], 0, v[130:131]
	v_lshlrev_b64 v[10:11], 12, v[8:9]
	v_lshl_add_u64 v[10:11], v[6:7], 0, v[10:11]
	v_or_b32_e32 v8, 8, v12
	s_waitcnt lgkmcnt(0)
	global_store_dwordx4 v[10:11], v[2:5], off
	s_nop 1
	v_lshl_add_u32 v2, v8, 7, v13
	ds_read_b128 v[2:5], v2
	v_or_b32_e32 v8, s0, v8
	v_lshlrev_b64 v[10:11], 12, v[8:9]
	v_lshl_add_u64 v[10:11], v[6:7], 0, v[10:11]
	v_or_b32_e32 v8, 16, v12
	s_waitcnt lgkmcnt(0)
	global_store_dwordx4 v[10:11], v[2:5], off
	s_nop 1
	v_lshl_add_u32 v2, v8, 7, v13
	ds_read_b128 v[2:5], v2
	v_or_b32_e32 v8, s0, v8
	v_lshlrev_b64 v[10:11], 12, v[8:9]
	v_lshl_add_u64 v[10:11], v[6:7], 0, v[10:11]
	v_or_b32_e32 v8, 24, v12
	s_waitcnt lgkmcnt(0)
	global_store_dwordx4 v[10:11], v[2:5], off
	s_nop 1
	v_lshl_add_u32 v2, v8, 7, v13
	ds_read_b128 v[2:5], v2
	v_or_b32_e32 v8, s0, v8
	v_lshlrev_b64 v[8:9], 12, v[8:9]
	v_lshl_add_u64 v[6:7], v[6:7], 0, v[8:9]
	s_waitcnt lgkmcnt(0)
	global_store_dwordx4 v[6:7], v[2:5], off
	s_waitcnt lgkmcnt(0)
	s_barrier
	s_setprio 0
	v_readlane_b32 s42, v249, 26
	v_readlane_b32 s50, v249, 30
	s_cmp_gt_i32 s60, 7
	v_readlane_b32 s43, v249, 27
	v_readlane_b32 s51, v249, 31
	s_cbranch_scc1 .LBB0_2336
	s_mul_i32 s0, s60, 48
	v_readlane_b32 s1, v248, 47
	s_add_i32 s6, s1, s0
	v_readlane_b32 s1, v248, 48
	s_add_i32 s0, s6, 48
	s_cmp_lg_u32 s60, 0
	v_mov_b32_e32 v2, s1
	v_min3_i32 v2, s0, v2, v165
	s_nop 0
	v_readfirstlane_b32 s26, v2
	s_waitcnt vmcnt(0)
	s_barrier
	s_cbranch_scc1 .LBB0_2595
	v_mov_b32_e32 v109, v0
	v_readlane_b32 s0, v248, 56
	v_lshlrev_b32_e32 v2, 2, v109
	v_ashrrev_i32_e32 v3, 31, v2
	v_readlane_b32 s1, v248, 57
	s_barrier
	s_nop 0
	v_lshl_add_u64 v[2:3], v[2:3], 2, s[0:1]
	global_load_dwordx4 v[32:35], v[2:3], off
	v_add_co_u32_e32 v4, vcc, 0x2000, v2
	s_movk_i32 s0, 0x4000
	s_nop 0
	v_addc_co_u32_e32 v5, vcc, 0, v3, vcc
	global_load_dwordx4 v[26:29], v[4:5], off
	v_add_co_u32_e32 v4, vcc, s0, v2
	v_lshl_add_u32 v30, v109, 4, 0
	s_nop 0
	v_addc_co_u32_e32 v5, vcc, 0, v3, vcc
	global_load_dwordx4 v[22:25], v[4:5], off
	v_add_co_u32_e32 v4, vcc, 0x6000, v2
	v_readlane_b32 s0, v248, 49
	s_nop 0
	v_addc_co_u32_e32 v5, vcc, 0, v3, vcc
	global_load_dwordx4 v[18:21], v[4:5], off
	v_add_co_u32_e32 v4, vcc, 0x8000, v2
	v_readlane_b32 s1, v248, 50
	s_nop 0
	v_addc_co_u32_e32 v5, vcc, 0, v3, vcc
	global_load_dwordx4 v[14:17], v[4:5], off
	v_add_co_u32_e32 v4, vcc, 0xa000, v2
	v_readlane_b32 s2, v248, 58
	s_nop 0
	v_addc_co_u32_e32 v5, vcc, 0, v3, vcc
	global_load_dwordx4 v[10:13], v[4:5], off
	v_add_co_u32_e32 v4, vcc, 0xc000, v2
	v_readlane_b32 s3, v248, 59
	s_nop 0
	v_addc_co_u32_e32 v5, vcc, 0, v3, vcc
	global_load_dwordx4 v[6:9], v[4:5], off
	v_add_co_u32_e32 v2, vcc, 0xe000, v2
	s_waitcnt vmcnt(6)
	v_mul_f32_e32 v31, 0xbfb8aa3b, v32
	v_exp_f32_e32 v31, v31
	v_addc_co_u32_e32 v3, vcc, 0, v3, vcc
	global_load_dwordx4 v[2:5], v[2:3], off
	v_add_f32_e32 v31, 1.0, v31
	v_rcp_f32_e32 v36, v31
	v_mul_f32_e32 v31, 0xbfb8aa3b, v33
	v_exp_f32_e32 v31, v31
	s_andn2_b64 vcc, exec, s[0:1]
	v_add_f32_e32 v31, 1.0, v31
	v_rcp_f32_e32 v37, v31
	v_mul_f32_e32 v31, 0xbfb8aa3b, v34
	v_exp_f32_e32 v31, v31
	v_pk_mul_f32 v[32:33], v[32:33], v[36:37]
	v_add_f32_e32 v31, 1.0, v31
	v_rcp_f32_e32 v38, v31
	v_mul_f32_e32 v31, 0xbfb8aa3b, v35
	v_exp_f32_e32 v31, v31
	s_nop 0
	v_add_f32_e32 v31, 1.0, v31
	v_rcp_f32_e32 v39, v31
	s_waitcnt vmcnt(6)
	v_mul_f32_e32 v31, 0xbfb8aa3b, v26
	v_exp_f32_e32 v31, v31
	v_pk_mul_f32 v[34:35], v[34:35], v[38:39]
	ds_write_b128 v30, v[32:35]
	v_add_f32_e32 v31, 1.0, v31
	v_rcp_f32_e32 v32, v31
	v_mul_f32_e32 v31, 0xbfb8aa3b, v27
	v_exp_f32_e32 v31, v31
	s_nop 0
	v_add_f32_e32 v31, 1.0, v31
	v_rcp_f32_e32 v33, v31
	v_mul_f32_e32 v31, 0xbfb8aa3b, v28
	v_exp_f32_e32 v31, v31
	v_pk_mul_f32 v[26:27], v[26:27], v[32:33]
	v_add_f32_e32 v31, 1.0, v31
	v_rcp_f32_e32 v34, v31
	v_mul_f32_e32 v31, 0xbfb8aa3b, v29
	v_exp_f32_e32 v31, v31
	s_nop 0
	v_add_f32_e32 v31, 1.0, v31
	v_rcp_f32_e32 v35, v31
	s_nop 0
	v_pk_mul_f32 v[28:29], v[28:29], v[34:35]
	ds_write_b128 v30, v[26:29] offset:8192
	s_waitcnt vmcnt(5)
	v_mul_f32_e32 v26, 0xbfb8aa3b, v22
	v_mul_f32_e32 v27, 0xbfb8aa3b, v23
	v_mul_f32_e32 v28, 0xbfb8aa3b, v24
	v_mul_f32_e32 v29, 0xbfb8aa3b, v25
	v_exp_f32_e32 v26, v26
	v_exp_f32_e32 v27, v27
	v_exp_f32_e32 v28, v28
	v_exp_f32_e32 v29, v29
	v_add_f32_e32 v26, 1.0, v26
	v_add_f32_e32 v27, 1.0, v27
	v_add_f32_e32 v28, 1.0, v28
	v_add_f32_e32 v29, 1.0, v29
	v_rcp_f32_e32 v26, v26
	v_rcp_f32_e32 v27, v27
	v_rcp_f32_e32 v28, v28
	v_rcp_f32_e32 v29, v29
	v_pk_mul_f32 v[22:23], v[22:23], v[26:27]
	v_pk_mul_f32 v[24:25], v[24:25], v[28:29]
	ds_write_b128 v30, v[22:25] offset:16384
	s_waitcnt vmcnt(4)
	v_mul_f32_e32 v22, 0xbfb8aa3b, v18
	v_mul_f32_e32 v23, 0xbfb8aa3b, v19
	v_mul_f32_e32 v24, 0xbfb8aa3b, v20
	v_mul_f32_e32 v25, 0xbfb8aa3b, v21
	v_exp_f32_e32 v22, v22
	v_exp_f32_e32 v23, v23
	v_exp_f32_e32 v24, v24
	v_exp_f32_e32 v25, v25
	v_add_f32_e32 v22, 1.0, v22
	v_add_f32_e32 v23, 1.0, v23
	v_add_f32_e32 v24, 1.0, v24
	v_add_f32_e32 v25, 1.0, v25
	v_rcp_f32_e32 v22, v22
	v_rcp_f32_e32 v23, v23
	v_rcp_f32_e32 v24, v24
	v_rcp_f32_e32 v25, v25
	v_pk_mul_f32 v[18:19], v[18:19], v[22:23]
	v_pk_mul_f32 v[20:21], v[20:21], v[24:25]
	ds_write_b128 v30, v[18:21] offset:24576
	s_waitcnt vmcnt(3)
	v_mul_f32_e32 v18, 0xbfb8aa3b, v14
	v_mul_f32_e32 v19, 0xbfb8aa3b, v15
	v_mul_f32_e32 v20, 0xbfb8aa3b, v16
	v_mul_f32_e32 v21, 0xbfb8aa3b, v17
	v_exp_f32_e32 v18, v18
	v_exp_f32_e32 v19, v19
	v_exp_f32_e32 v20, v20
	v_exp_f32_e32 v21, v21
	v_add_f32_e32 v18, 1.0, v18
	v_add_f32_e32 v19, 1.0, v19
	v_add_f32_e32 v20, 1.0, v20
	v_add_f32_e32 v21, 1.0, v21
	v_rcp_f32_e32 v18, v18
	v_rcp_f32_e32 v19, v19
	v_rcp_f32_e32 v20, v20
	v_rcp_f32_e32 v21, v21
	v_pk_mul_f32 v[14:15], v[14:15], v[18:19]
	v_pk_mul_f32 v[16:17], v[16:17], v[20:21]
	ds_write_b128 v30, v[14:17] offset:32768
	s_waitcnt vmcnt(2)
	v_mul_f32_e32 v14, 0xbfb8aa3b, v10
	v_mul_f32_e32 v15, 0xbfb8aa3b, v11
	v_mul_f32_e32 v16, 0xbfb8aa3b, v12
	v_mul_f32_e32 v17, 0xbfb8aa3b, v13
	v_exp_f32_e32 v14, v14
	v_exp_f32_e32 v15, v15
	v_exp_f32_e32 v16, v16
	v_exp_f32_e32 v17, v17
	v_add_f32_e32 v14, 1.0, v14
	v_add_f32_e32 v15, 1.0, v15
	v_add_f32_e32 v16, 1.0, v16
	v_add_f32_e32 v17, 1.0, v17
	v_rcp_f32_e32 v14, v14
	v_rcp_f32_e32 v15, v15
	v_rcp_f32_e32 v16, v16
	v_rcp_f32_e32 v17, v17
	v_pk_mul_f32 v[10:11], v[10:11], v[14:15]
	v_pk_mul_f32 v[12:13], v[12:13], v[16:17]
	ds_write_b128 v30, v[10:13] offset:40960
	s_waitcnt vmcnt(1)
	v_mul_f32_e32 v10, 0xbfb8aa3b, v6
	v_mul_f32_e32 v11, 0xbfb8aa3b, v7
	v_mul_f32_e32 v12, 0xbfb8aa3b, v8
	v_mul_f32_e32 v13, 0xbfb8aa3b, v9
	v_exp_f32_e32 v10, v10
	v_exp_f32_e32 v11, v11
	v_exp_f32_e32 v12, v12
	v_exp_f32_e32 v13, v13
	v_add_f32_e32 v10, 1.0, v10
	v_add_f32_e32 v11, 1.0, v11
	v_add_f32_e32 v12, 1.0, v12
	v_add_f32_e32 v13, 1.0, v13
	v_rcp_f32_e32 v10, v10
	v_rcp_f32_e32 v11, v11
	v_rcp_f32_e32 v12, v12
	v_rcp_f32_e32 v13, v13
	v_pk_mul_f32 v[6:7], v[6:7], v[10:11]
	v_pk_mul_f32 v[8:9], v[8:9], v[12:13]
	ds_write_b128 v30, v[6:9] offset:49152
	s_waitcnt vmcnt(0)
	v_mul_f32_e32 v6, 0xbfb8aa3b, v2
	v_mul_f32_e32 v7, 0xbfb8aa3b, v3
	v_mul_f32_e32 v8, 0xbfb8aa3b, v4
	v_mul_f32_e32 v9, 0xbfb8aa3b, v5
	v_exp_f32_e32 v6, v6
	v_exp_f32_e32 v7, v7
	v_exp_f32_e32 v8, v8
	v_exp_f32_e32 v9, v9
	v_add_f32_e32 v6, 1.0, v6
	v_add_f32_e32 v7, 1.0, v7
	v_add_f32_e32 v8, 1.0, v8
	v_add_f32_e32 v9, 1.0, v9
	v_rcp_f32_e32 v6, v6
	v_rcp_f32_e32 v7, v7
	v_rcp_f32_e32 v8, v8
	v_rcp_f32_e32 v9, v9
	v_pk_mul_f32 v[2:3], v[2:3], v[6:7]
	v_pk_mul_f32 v[4:5], v[4:5], v[8:9]
	ds_write_b128 v30, v[2:5] offset:57344
	s_waitcnt lgkmcnt(0)
	s_barrier
	s_cbranch_vccnz .LBB0_2595
	s_movk_i32 s0, 0x1f8
	v_cmp_gt_i32_e32 vcc, s0, v109
	s_mov_b32 s0, 0x2aaaaaab
	v_mul_hi_i32 v111, v109, s0
	v_lshrrev_b32_e32 v113, 31, v111
	s_and_saveexec_b64 s[0:1], vcc
	s_cbranch_execz .LBB0_2592
	v_ashrrev_i32_e32 v2, 1, v111
	v_add_u32_e32 v115, v2, v113
	v_mul_lo_u32 v2, v115, 12
	v_sub_u32_e32 v2, v109, v2
	v_lshlrev_b32_e32 v2, 2, v2
	v_readlane_b32 s2, v248, 60
	v_ashrrev_i32_e32 v3, 31, v2
	v_readlane_b32 s3, v248, 61
	s_mov_b32 s4, 0xc000
	v_add_u32_e32 v117, 42, v115
	v_lshl_add_u64 v[62:63], v[2:3], 2, s[2:3]
	v_add_u32_e32 v119, 0x54, v115
	v_add_u32_e32 v121, 0x7e, v115
	v_add_u32_e32 v123, 0xa8, v115
	v_add_u32_e32 v125, 0xd2, v115
	v_add_u32_e32 v127, 0xfc, v115
	v_mad_i64_i32 v[2:3], s[2:3], v115, s4, v[62:63]
	v_mad_i64_i32 v[6:7], s[2:3], v117, s4, v[62:63]
	v_mad_i64_i32 v[10:11], s[2:3], v119, s4, v[62:63]
	v_mad_i64_i32 v[14:15], s[2:3], v121, s4, v[62:63]
	v_mad_i64_i32 v[18:19], s[2:3], v123, s4, v[62:63]
	v_mad_i64_i32 v[22:23], s[2:3], v125, s4, v[62:63]
	v_mad_i64_i32 v[26:27], s[2:3], v127, s4, v[62:63]
	global_load_dwordx4 v[2:5], v[2:3], off nt
	v_mov_b32_e32 v30, 0
	global_load_dwordx4 v[6:9], v[6:7], off nt
	s_mov_b32 s2, 0
	global_load_dwordx4 v[10:13], v[10:11], off nt
	v_mov_b32_e32 v31, v30
	global_load_dwordx4 v[14:17], v[14:15], off nt
	v_mov_b32_e32 v32, v30
	global_load_dwordx4 v[18:21], v[18:19], off nt
	v_mov_b32_e32 v33, v30
	global_load_dwordx4 v[22:25], v[22:23], off nt
	v_mov_b32_e32 v54, v30
	global_load_dwordx4 v[26:29], v[26:27], off nt
	v_mov_b32_e32 v55, v30
	v_mov_b32_e32 v56, v30
	v_mov_b32_e32 v57, v30
	v_mov_b32_e32 v50, v30
	v_mov_b32_e32 v51, v30
	v_mov_b32_e32 v52, v30
	v_mov_b32_e32 v53, v30
	v_mov_b32_e32 v46, v30
	v_mov_b32_e32 v47, v30
	v_mov_b32_e32 v48, v30
	v_mov_b32_e32 v49, v30
	v_mov_b32_e32 v42, v30
	v_mov_b32_e32 v43, v30
	v_mov_b32_e32 v44, v30
	v_mov_b32_e32 v45, v30
	v_mov_b32_e32 v38, v30
	v_mov_b32_e32 v39, v30
	v_mov_b32_e32 v40, v30
	v_mov_b32_e32 v41, v30
	v_mov_b32_e32 v34, v30
	v_mov_b32_e32 v35, v30
	v_mov_b32_e32 v36, v30
	v_mov_b32_e32 v37, v30
	v_mov_b32_e32 v58, v30
	v_mov_b32_e32 v59, v30
	v_mov_b32_e32 v60, v30
	v_mov_b32_e32 v61, v30
	s_waitcnt vmcnt(6)
	v_mov_b32_e32 v64, v2
	v_mov_b32_e32 v65, v3
	v_mov_b32_e32 v82, v4
	v_mov_b32_e32 v83, v5
	s_waitcnt vmcnt(5)
	v_mov_b32_e32 v84, v6
	v_mov_b32_e32 v85, v7
	v_mov_b32_e32 v86, v8
	v_mov_b32_e32 v87, v9
	s_waitcnt vmcnt(4)
	v_mov_b32_e32 v88, v10
	v_mov_b32_e32 v89, v11
	v_mov_b32_e32 v90, v12
	v_mov_b32_e32 v91, v13
	s_waitcnt vmcnt(3)
	v_mov_b32_e32 v92, v14
	v_mov_b32_e32 v93, v15
	v_mov_b32_e32 v94, v16
	v_mov_b32_e32 v95, v17
	s_waitcnt vmcnt(2)
	v_mov_b32_e32 v96, v18
	v_mov_b32_e32 v97, v19
	v_mov_b32_e32 v98, v20
	v_mov_b32_e32 v99, v21
	s_waitcnt vmcnt(1)
	v_mov_b32_e32 v100, v22
	v_mov_b32_e32 v101, v23
	v_mov_b32_e32 v102, v24
	v_mov_b32_e32 v103, v25
	s_waitcnt vmcnt(0)
	v_mov_b32_e32 v104, v26
	v_mov_b32_e32 v105, v27
	v_mov_b32_e32 v106, v28
	v_mov_b32_e32 v107, v29
	s_branch .LBB0_2477

.LBB0_2595:
	v_readlane_b32 s7, v249, 16
	s_mov_b32 s27, s26
	s_nop 0
	s_add_i32 s25, s6, s7
	v_readlane_b32 s12, v244, 2
	s_mov_b32 s13, 0
	s_lshr_b32 s12, s12, 2
	s_lshl_b32 s12, s12, 3
	s_add_i32 s25, s25, s12
	v_writelane_b32 v244, s13, 2
	s_cmp_ge_i32 s25, s27
	s_cbranch_scc1 .LBB0_2335
	v_and_b32_e32 v36, 63, v0
	v_lshrrev_b32_e32 v37, 3, v36
	v_and_b32_e32 v38, 7, v36
	v_lshlrev_b32_e32 v38, 4, v38
	v_lshl_add_u32 v82, v37, 11, v38
	v_lshl_add_u32 v83, v37, 13, v38
	v_and_b32_e32 v37, 3, v36
	v_lshrrev_b32_e32 v38, 2, v36
	v_mul_u32_u24_e32 v84, 0x820, v37
	v_lshl_add_u32 v84, v38, 2, v84
	v_lshlrev_b32_e32 v85, 4, v37
	v_lshl_add_u32 v86, v38, 11, v85
	v_lshl_add_u32 v87, v38, 9, v85
	v_mov_b32_e32 v100, 0x42800000
	v_mov_b32_e32 v101, 0x42800000
	v_readlane_b32 s8, v249, 1
	v_readlane_b32 s9, v249, 2
	s_lshl_b32 s72, s7, 1
	s_mul_i32 s72, s72, 8320
	s_add_i32 s86, s72, 8320
	s_cmp_eq_u32 s7, 7
	s_cselect_b32 s86, 0x24000, s86
	s_load_dwordx2 s[10:11], s[8:9], 0xe0
	s_mov_b32 s32, 0
	s_waitcnt lgkmcnt(0)
	s_sub_u32 s7, s25, 0x3e90
	s_lshr_b32 vcc_lo, s7, 15
	s_and_b32 s7, s7, 0x7fff
	s_lshl_b32 vcc_hi, vcc_lo, 3
	s_addk_i32 vcc_hi, 0xa8
	s_load_dwordx2 s[70:71], s[8:9], vcc_hi
	s_lshr_b32 vcc_hi, s7, 9
	s_and_b32 s7, s7, 0x1ff
	s_cmp_eq_u32 vcc_lo, 2
	s_cbranch_scc1 .Lcvdb_pdn
	s_lshr_b32 s13, s7, 4
	s_and_b32 s7, s7, 15
	s_lshl_b32 s100, vcc_hi, 21
	s_lshl_b32 s101, vcc_hi, 22
	s_lshl_b32 vcc_hi, s13, 6
	s_add_u32 s100, s100, vcc_hi
	s_lshl_b32 vcc_hi, s13, 17
	s_add_u32 s101, s101, vcc_hi
	s_lshl_b32 vcc_hi, s7, 7
	s_add_u32 s101, s101, vcc_hi
	s_lshr_b32 vcc_hi, s7, 2
	s_lshl_b32 vcc_hi, vcc_hi, 19
	s_add_u32 s100, s100, vcc_hi
	s_and_b32 vcc_hi, s7, 3
	s_lshl_b32 vcc_hi, vcc_hi, 16
	s_add_u32 s100, s100, vcc_hi
	s_lshl_b32 vcc_hi, vcc_lo, 18
	s_add_u32 s100, s100, vcc_hi
	s_add_u32 s100, s100, 0x1b000000
	s_mov_b32 s61, 0x4000
	s_mov_b32 s99, 0
	s_branch .Lcvdb_pdd
